# adds attention epilogue gain-load pipelining and conv-row load waits moved to consumers
# baseline (speedup 1.0000x reference)
.LBB0_315:
	ds_bpermute_b32 v2, v197, v5
	v_ashrrev_i32_e32 v195, 31, v194
	s_waitcnt lgkmcnt(0)
	v_add_f32_e32 v2, v5, v2
	v_div_scale_f32 v4, s[8:9], v2, v2, 1.0
	v_rcp_f32_e32 v5, v4
	s_nop 0
	v_fma_f32 v6, -v4, v5, 1.0
	v_fmac_f32_e32 v5, v6, v5
	v_div_scale_f32 v6, vcc, 1.0, v2, 1.0
	v_mul_f32_e32 v7, v6, v5
	v_fma_f32 v8, -v4, v7, v6
	v_fmac_f32_e32 v7, v8, v5
	v_fma_f32 v4, -v4, v7, v6
	v_div_fmas_f32 v4, v4, v5, v7
	v_div_fixup_f32 v4, v4, v2, 1.0
	v_mul_f32_e32 v86, v67, v4
	v_mul_f32_e32 v87, v66, v4
	v_mul_f32_e32 v14, v86, v86
	v_fmac_f32_e32 v14, v87, v87
	v_mul_f32_e32 v88, v68, v4
	v_fmac_f32_e32 v14, v88, v88
	v_mul_f32_e32 v89, v69, v4
	v_fmac_f32_e32 v14, v89, v89
	v_mul_f32_e32 v6, v70, v4
	v_fmac_f32_e32 v14, v6, v6
	v_mul_f32_e32 v84, v71, v4
	v_fmac_f32_e32 v14, v84, v84
	v_mul_f32_e32 v83, v72, v4
	v_fmac_f32_e32 v14, v83, v83
	v_mul_f32_e32 v85, v73, v4
	v_fmac_f32_e32 v14, v85, v85
	v_mul_f32_e32 v8, v74, v4
	v_fmac_f32_e32 v14, v8, v8
	v_mul_f32_e32 v10, v75, v4
	v_fmac_f32_e32 v14, v10, v10
	v_mul_f32_e32 v9, v76, v4
	v_fmac_f32_e32 v14, v9, v9
	v_mul_f32_e32 v11, v77, v4
	v_fmac_f32_e32 v14, v11, v11
	v_mul_f32_e32 v7, v78, v4
	v_fmac_f32_e32 v14, v7, v7
	v_mul_f32_e32 v79, v79, v4
	v_fmac_f32_e32 v14, v79, v79
	v_mul_f32_e32 v78, v80, v4
	v_fmac_f32_e32 v14, v78, v78
	v_mul_f32_e32 v80, v81, v4
	v_fmac_f32_e32 v14, v80, v80
	v_mul_f32_e32 v74, v50, v4
	v_fmac_f32_e32 v14, v74, v74
	v_mul_f32_e32 v76, v51, v4
	v_fmac_f32_e32 v14, v76, v76
	v_mul_f32_e32 v75, v52, v4
	v_fmac_f32_e32 v14, v75, v75
	v_mul_f32_e32 v77, v53, v4
	v_fmac_f32_e32 v14, v77, v77
	v_mul_f32_e32 v70, v54, v4
	v_fmac_f32_e32 v14, v70, v70
	v_mul_f32_e32 v72, v55, v4
	v_fmac_f32_e32 v14, v72, v72
	v_mul_f32_e32 v71, v56, v4
	v_fmac_f32_e32 v14, v71, v71
	v_mul_f32_e32 v73, v57, v4
	v_fmac_f32_e32 v14, v73, v73
	v_mul_f32_e32 v66, v58, v4
	v_fmac_f32_e32 v14, v66, v66
	v_mul_f32_e32 v68, v59, v4
	v_fmac_f32_e32 v14, v68, v68
	v_mul_f32_e32 v67, v60, v4
	v_fmac_f32_e32 v14, v67, v67
	v_mul_f32_e32 v69, v61, v4
	v_fmac_f32_e32 v14, v69, v69
	v_mul_f32_e32 v60, v62, v4
	v_fmac_f32_e32 v14, v60, v60
	v_mul_f32_e32 v62, v63, v4
	v_fmac_f32_e32 v14, v62, v62
	v_mul_f32_e32 v61, v64, v4
	v_fmac_f32_e32 v14, v61, v61
	v_mul_f32_e32 v63, v65, v4
	v_fmac_f32_e32 v14, v63, v63
	v_mul_f32_e32 v56, v34, v4
	v_fmac_f32_e32 v14, v56, v56
	v_mul_f32_e32 v58, v35, v4
	v_fmac_f32_e32 v14, v58, v58
	v_mul_f32_e32 v57, v36, v4
	v_fmac_f32_e32 v14, v57, v57
	v_mul_f32_e32 v59, v37, v4
	v_fmac_f32_e32 v14, v59, v59
	v_mul_f32_e32 v52, v38, v4
	v_fmac_f32_e32 v14, v52, v52
	v_mul_f32_e32 v54, v39, v4
	v_fmac_f32_e32 v14, v54, v54
	v_mul_f32_e32 v53, v40, v4
	v_fmac_f32_e32 v14, v53, v53
	v_mul_f32_e32 v55, v41, v4
	v_fmac_f32_e32 v14, v55, v55
	v_mul_f32_e32 v50, v42, v4
	v_fmac_f32_e32 v14, v50, v50
	v_mul_f32_e32 v51, v43, v4
	v_fmac_f32_e32 v14, v51, v51
	v_mul_f32_e32 v44, v44, v4
	v_fmac_f32_e32 v14, v44, v44
	v_mul_f32_e32 v45, v45, v4
	v_fmac_f32_e32 v14, v45, v45
	v_mul_f32_e32 v40, v46, v4
	v_fmac_f32_e32 v14, v40, v40
	v_mul_f32_e32 v42, v47, v4
	v_fmac_f32_e32 v14, v42, v42
	v_mul_f32_e32 v41, v48, v4
	v_fmac_f32_e32 v14, v41, v41
	v_mul_f32_e32 v43, v49, v4
	v_fmac_f32_e32 v14, v43, v43
	v_mul_f32_e32 v36, v18, v4
	v_fmac_f32_e32 v14, v36, v36
	v_mul_f32_e32 v39, v19, v4
	v_fmac_f32_e32 v14, v39, v39
	v_mul_f32_e32 v37, v20, v4
	v_fmac_f32_e32 v14, v37, v37
	v_mul_f32_e32 v38, v21, v4
	v_fmac_f32_e32 v14, v38, v38
	v_mul_f32_e32 v34, v22, v4
	v_fmac_f32_e32 v14, v34, v34
	v_mul_f32_e32 v35, v23, v4
	v_fmac_f32_e32 v14, v35, v35
	v_mul_f32_e32 v24, v24, v4
	v_fmac_f32_e32 v14, v24, v24
	v_mul_f32_e32 v25, v25, v4
	v_fmac_f32_e32 v14, v25, v25
	v_mul_f32_e32 v22, v26, v4
	v_fmac_f32_e32 v14, v22, v22
	v_mul_f32_e32 v23, v27, v4
	v_fmac_f32_e32 v14, v23, v23
	v_mul_f32_e32 v20, v28, v4
	v_fmac_f32_e32 v14, v20, v20
	v_mul_f32_e32 v21, v29, v4
	v_fmac_f32_e32 v14, v21, v21
	v_mul_f32_e32 v2, v30, v4
	v_fmac_f32_e32 v14, v2, v2
	v_mul_f32_e32 v18, v31, v4
	v_pk_mul_f32 v[12:13], v[32:33], v[4:5] op_sel_hi:[1,0]
	v_fmac_f32_e32 v14, v18, v18
	v_pk_mul_f32 v[4:5], v[12:13], v[12:13]
	s_nop 0
	v_add_f32_e32 v4, v4, v14
	v_add_f32_e32 v4, v5, v4
	ds_bpermute_b32 v5, v197, v4
	s_waitcnt lgkmcnt(0)
	v_add_f32_e32 v4, v4, v5
	v_fmamk_f32 v4, v4, 0x3c000000, v207
	v_cmp_gt_f32_e32 vcc, s10, v4
	v_mul_f32_e32 v5, 0x4f800000, v4
	s_nop 0
	v_cndmask_b32_e32 v4, v4, v5, vcc
	v_sqrt_f32_e32 v5, v4
	s_nop 0
	v_add_u32_e32 v14, -1, v5
	v_fma_f32 v15, -v14, v5, v4
	v_cmp_ge_f32_e64 s[42:43], 0, v15
	v_add_u32_e32 v15, 1, v5
	s_nop 0
	v_cndmask_b32_e64 v14, v5, v14, s[42:43]
	v_fma_f32 v5, -v15, v5, v4
	v_cmp_lt_f32_e64 s[42:43], 0, v5
	s_nop 1
	v_cndmask_b32_e64 v5, v14, v15, s[42:43]
	v_mul_f32_e32 v14, 0x37800000, v5
	v_cndmask_b32_e32 v5, v5, v14, vcc
	v_cmp_class_f32_e32 vcc, v4, v208
	s_nop 1
	v_cndmask_b32_e32 v4, v5, v4, vcc
	v_div_scale_f32 v5, s[8:9], v4, v4, 1.0
	v_rcp_f32_e32 v14, v5
	s_lshl_b32 s8, s66, 7
	s_ashr_i32 s9, s8, 31
	s_mov_b32 s66, s67
	v_fma_f32 v15, -v5, v14, 1.0
	v_fmac_f32_e32 v14, v15, v14
	v_div_scale_f32 v15, vcc, 1.0, v4, 1.0
	v_mul_f32_e32 v16, v15, v14
	v_fma_f32 v17, -v5, v16, v15
	v_fmac_f32_e32 v16, v17, v14
	v_fma_f32 v5, -v5, v16, v15
	v_div_fmas_f32 v5, v5, v14, v16
	v_lshl_add_u64 v[16:17], s[8:9], 2, v[190:191]
	global_load_dwordx4 v[222:225], v[16:17], off
	global_load_dwordx4 v[226:229], v[16:17], off offset:32
	global_load_dwordx4 v[230:233], v[16:17], off offset:64
	global_load_dwordx4 v[234:237], v[16:17], off offset:96
	global_load_dwordx4 v[238:241], v[16:17], off offset:128
	global_load_dwordx4 v[242:245], v[16:17], off offset:160
	global_load_dwordx4 v[246:249], v[16:17], off offset:192
	v_div_fixup_f32 v19, v5, v4, 1.0
	v_lshlrev_b64 v[4:5], 11, v[194:195]
	v_lshl_add_u64 v[4:5], s[50:51], 0, v[4:5]
	v_lshl_add_u64 v[4:5], v[4:5], 0, s[8:9]
	v_lshl_add_u64 v[14:15], v[4:5], 0, v[182:183]
	v_mul_f32_e32 v4, v87, v19
	v_mul_f32_e32 v7, v7, v19
	v_mul_f32_e32 v2, v2, v19
	s_andn2_b64 vcc, exec, s[52:53]
	v_mov_b32_e32 v194, v82
	s_waitcnt vmcnt(6)
	s_nop 1
	v_mov_b32_e32 v26, v222
	v_mov_b32_e32 v27, v223
	v_mov_b32_e32 v28, v224
	v_mov_b32_e32 v29, v225
	global_load_dwordx4 v[222:225], v[16:17], off offset:224
	v_mul_f32_e32 v5, v26, v4
	v_mul_f32_e32 v4, v86, v19
	v_mul_f32_e32 v26, v27, v4
	v_mov_b32_e32 v4, v3
	v_cvt_pk_fp8_f32 v4, v5, v26
	v_mul_f32_e32 v5, v88, v19
	v_mul_f32_e32 v26, v89, v19
	v_mul_f32_e32 v5, v28, v5
	v_mul_f32_e32 v26, v29, v26
	v_cvt_pk_fp8_f32 v4, v5, v26 op_sel:[0,0,1]
	v_mul_f32_e32 v5, v6, v19
	v_mul_f32_e32 v6, v84, v19
	s_waitcnt vmcnt(6)
	s_nop 1
	v_mov_b32_e32 v26, v226
	v_mov_b32_e32 v27, v227
	v_mov_b32_e32 v28, v228
	v_mov_b32_e32 v29, v229
	global_load_dwordx4 v[226:229], v[16:17], off offset:256
	v_mul_f32_e32 v5, v26, v5
	v_mul_f32_e32 v26, v27, v6
	v_mov_b32_e32 v6, v3
	v_cvt_pk_fp8_f32 v6, v5, v26
	v_mul_f32_e32 v5, v83, v19
	v_mul_f32_e32 v26, v85, v19
	v_mul_f32_e32 v5, v28, v5
	v_mul_f32_e32 v26, v29, v26
	v_cvt_pk_fp8_f32 v6, v5, v26 op_sel:[0,0,1]
	v_mul_f32_e32 v5, v8, v19
	s_waitcnt vmcnt(6)
	s_nop 1
	v_mov_b32_e32 v26, v230
	v_mov_b32_e32 v27, v231
	v_mov_b32_e32 v28, v232
	v_mov_b32_e32 v29, v233
	global_load_dwordx4 v[230:233], v[16:17], off offset:288
	v_mul_f32_e32 v8, v26, v5
	v_mul_f32_e32 v5, v10, v19
	v_mul_f32_e32 v10, v27, v5
	v_mov_b32_e32 v5, v3
	v_cvt_pk_fp8_f32 v5, v8, v10
	v_mul_f32_e32 v8, v9, v19
	v_mul_f32_e32 v9, v11, v19
	v_mul_f32_e32 v8, v28, v8
	v_mul_f32_e32 v9, v29, v9
	v_cvt_pk_fp8_f32 v5, v8, v9 op_sel:[0,0,1]
	s_nop 0
	v_permlane32_swap_b32_e32 v4, v5
	s_waitcnt vmcnt(6)
	s_nop 1
	v_mov_b32_e32 v8, v234
	v_mov_b32_e32 v9, v235
	v_mov_b32_e32 v10, v236
	v_mov_b32_e32 v11, v237
	global_load_dwordx4 v[234:237], v[16:17], off offset:320
	v_mul_f32_e32 v8, v8, v7
	v_mul_f32_e32 v7, v79, v19
	v_mul_f32_e32 v9, v9, v7
	v_mov_b32_e32 v7, v3
	v_cvt_pk_fp8_f32 v7, v8, v9
	v_mul_f32_e32 v8, v78, v19
	v_mul_f32_e32 v9, v80, v19
	v_mul_f32_e32 v8, v10, v8
	v_mul_f32_e32 v9, v11, v9
	v_cvt_pk_fp8_f32 v7, v8, v9 op_sel:[0,0,1]
	v_mul_f32_e32 v8, v74, v19
	s_nop 0
	v_permlane32_swap_b32_e32 v6, v7
	global_store_dwordx4 v[14:15], v[4:7], off
	s_waitcnt vmcnt(7)
	s_nop 1
	v_mov_b32_e32 v4, v238
	v_mov_b32_e32 v5, v239
	v_mov_b32_e32 v6, v240
	v_mov_b32_e32 v7, v241
	global_load_dwordx4 v[238:241], v[16:17], off offset:352
	v_mul_f32_e32 v8, v4, v8
	v_mul_f32_e32 v4, v76, v19
	v_mul_f32_e32 v5, v5, v4
	v_mov_b32_e32 v4, v3
	v_cvt_pk_fp8_f32 v4, v8, v5
	v_mul_f32_e32 v5, v75, v19
	v_mul_f32_e32 v5, v6, v5
	v_mul_f32_e32 v6, v77, v19
	v_mul_f32_e32 v6, v7, v6
	v_cvt_pk_fp8_f32 v4, v5, v6 op_sel:[0,0,1]
	v_mul_f32_e32 v5, v70, v19
	s_waitcnt vmcnt(7)
	s_nop 1
	v_mov_b32_e32 v6, v242
	v_mov_b32_e32 v7, v243
	v_mov_b32_e32 v8, v244
	v_mov_b32_e32 v9, v245
	global_load_dwordx4 v[242:245], v[16:17], off offset:384
	v_mul_f32_e32 v5, v6, v5
	v_mul_f32_e32 v6, v72, v19
	v_mul_f32_e32 v7, v7, v6
	v_mov_b32_e32 v6, v3
	v_cvt_pk_fp8_f32 v6, v5, v7
	v_mul_f32_e32 v5, v71, v19
	v_mul_f32_e32 v7, v73, v19
	v_mul_f32_e32 v5, v8, v5
	v_mul_f32_e32 v7, v9, v7
	v_cvt_pk_fp8_f32 v6, v5, v7 op_sel:[0,0,1]
	v_mul_f32_e32 v5, v66, v19
	s_waitcnt vmcnt(7)
	s_nop 1
	v_mov_b32_e32 v8, v246
	v_mov_b32_e32 v9, v247
	v_mov_b32_e32 v10, v248
	v_mov_b32_e32 v11, v249
	global_load_dwordx4 v[246:249], v[16:17], off offset:416
	v_mul_f32_e32 v7, v8, v5
	v_mul_f32_e32 v5, v68, v19
	v_mul_f32_e32 v8, v9, v5
	v_mov_b32_e32 v5, v3
	v_cvt_pk_fp8_f32 v5, v7, v8
	v_mul_f32_e32 v7, v67, v19
	v_mul_f32_e32 v8, v69, v19
	v_mul_f32_e32 v7, v10, v7
	v_mul_f32_e32 v8, v11, v8
	v_cvt_pk_fp8_f32 v5, v7, v8 op_sel:[0,0,1]
	v_mul_f32_e32 v7, v60, v19
	v_permlane32_swap_b32_e32 v4, v5
	s_waitcnt vmcnt(7)
	s_nop 1
	v_mov_b32_e32 v8, v222
	v_mov_b32_e32 v9, v223
	v_mov_b32_e32 v10, v224
	v_mov_b32_e32 v11, v225
	global_load_dwordx4 v[222:225], v[16:17], off offset:448
	v_mul_f32_e32 v8, v8, v7
	v_mul_f32_e32 v7, v62, v19
	v_mul_f32_e32 v9, v9, v7
	v_mov_b32_e32 v7, v3
	v_cvt_pk_fp8_f32 v7, v8, v9
	v_mul_f32_e32 v8, v61, v19
	v_mul_f32_e32 v9, v63, v19
	v_mul_f32_e32 v8, v10, v8
	v_mul_f32_e32 v9, v11, v9
	v_cvt_pk_fp8_f32 v7, v8, v9 op_sel:[0,0,1]
	v_mul_f32_e32 v8, v56, v19
	s_nop 0
	v_permlane32_swap_b32_e32 v6, v7
	global_store_dwordx4 v[14:15], v[4:7], off offset:32
	s_waitcnt vmcnt(8)
	s_nop 1
	v_mov_b32_e32 v4, v226
	v_mov_b32_e32 v5, v227
	v_mov_b32_e32 v6, v228
	v_mov_b32_e32 v7, v229
	global_load_dwordx4 v[226:229], v[16:17], off offset:480
	v_mul_f32_e32 v8, v4, v8
	v_mul_f32_e32 v4, v58, v19
	v_mul_f32_e32 v5, v5, v4
	v_mov_b32_e32 v4, v3
	v_cvt_pk_fp8_f32 v4, v8, v5
	v_mul_f32_e32 v5, v57, v19
	v_mul_f32_e32 v5, v6, v5
	v_mul_f32_e32 v6, v59, v19
	v_mul_f32_e32 v6, v7, v6
	v_cvt_pk_fp8_f32 v4, v5, v6 op_sel:[0,0,1]
	v_mul_f32_e32 v5, v52, v19
	s_waitcnt vmcnt(8)
	s_nop 1
	v_mov_b32_e32 v6, v230
	v_mov_b32_e32 v7, v231
	v_mov_b32_e32 v8, v232
	v_mov_b32_e32 v9, v233
	v_mul_f32_e32 v5, v6, v5
	v_mul_f32_e32 v6, v54, v19
	v_mul_f32_e32 v7, v7, v6
	v_mov_b32_e32 v6, v3
	v_cvt_pk_fp8_f32 v6, v5, v7
	v_mul_f32_e32 v5, v53, v19
	v_mul_f32_e32 v7, v55, v19
	v_mul_f32_e32 v5, v8, v5
	v_mul_f32_e32 v7, v9, v7
	v_cvt_pk_fp8_f32 v6, v5, v7 op_sel:[0,0,1]
	v_mul_f32_e32 v5, v50, v19
	s_waitcnt vmcnt(7)
	s_nop 1
	v_mov_b32_e32 v8, v234
	v_mov_b32_e32 v9, v235
	v_mov_b32_e32 v10, v236
	v_mov_b32_e32 v11, v237
	v_mul_f32_e32 v7, v8, v5
	v_mul_f32_e32 v5, v51, v19
	v_mul_f32_e32 v8, v9, v5
	v_mov_b32_e32 v5, v3
	v_cvt_pk_fp8_f32 v5, v7, v8
	v_mul_f32_e32 v7, v44, v19
	v_mul_f32_e32 v8, v45, v19
	v_mul_f32_e32 v7, v10, v7
	v_mul_f32_e32 v8, v11, v8
	v_cvt_pk_fp8_f32 v5, v7, v8 op_sel:[0,0,1]
	v_mul_f32_e32 v7, v40, v19
	v_permlane32_swap_b32_e32 v4, v5
	s_waitcnt vmcnt(5)
	s_nop 1
	v_mov_b32_e32 v8, v238
	v_mov_b32_e32 v9, v239
	v_mov_b32_e32 v10, v240
	v_mov_b32_e32 v11, v241
	v_mul_f32_e32 v8, v8, v7
	v_mul_f32_e32 v7, v42, v19
	v_mul_f32_e32 v9, v9, v7
	v_mov_b32_e32 v7, v3
	v_cvt_pk_fp8_f32 v7, v8, v9
	v_mul_f32_e32 v8, v41, v19
	v_mul_f32_e32 v9, v43, v19
	v_mul_f32_e32 v8, v10, v8
	v_mul_f32_e32 v9, v11, v9
	v_cvt_pk_fp8_f32 v7, v8, v9 op_sel:[0,0,1]
	v_mul_f32_e32 v8, v36, v19
	s_nop 0
	v_permlane32_swap_b32_e32 v6, v7
	global_store_dwordx4 v[14:15], v[4:7], off offset:64
	s_waitcnt vmcnt(5)
	s_nop 1
	v_mov_b32_e32 v4, v242
	v_mov_b32_e32 v5, v243
	v_mov_b32_e32 v6, v244
	v_mov_b32_e32 v7, v245
	v_mul_f32_e32 v8, v4, v8
	v_mul_f32_e32 v4, v39, v19
	v_mul_f32_e32 v5, v5, v4
	v_mov_b32_e32 v4, v3
	v_cvt_pk_fp8_f32 v4, v8, v5
	v_mul_f32_e32 v5, v37, v19
	v_mul_f32_e32 v5, v6, v5
	v_mul_f32_e32 v6, v38, v19
	v_mul_f32_e32 v6, v7, v6
	v_cvt_pk_fp8_f32 v4, v5, v6 op_sel:[0,0,1]
	v_mul_f32_e32 v5, v34, v19
	s_waitcnt vmcnt(4)
	s_nop 1
	v_mov_b32_e32 v6, v246
	v_mov_b32_e32 v7, v247
	v_mov_b32_e32 v8, v248
	v_mov_b32_e32 v9, v249
	v_mul_f32_e32 v5, v6, v5
	v_mul_f32_e32 v6, v35, v19
	v_mul_f32_e32 v7, v7, v6
	v_mov_b32_e32 v6, v3
	v_cvt_pk_fp8_f32 v6, v5, v7
	v_mul_f32_e32 v5, v24, v19
	v_mul_f32_e32 v7, v25, v19
	v_mul_f32_e32 v5, v8, v5
	v_mul_f32_e32 v7, v9, v7
	v_cvt_pk_fp8_f32 v6, v5, v7 op_sel:[0,0,1]
	v_mul_f32_e32 v5, v22, v19
	s_waitcnt vmcnt(3)
	s_nop 1
	v_mov_b32_e32 v8, v222
	v_mov_b32_e32 v9, v223
	v_mov_b32_e32 v10, v224
	v_mov_b32_e32 v11, v225
	v_mul_f32_e32 v7, v8, v5
	v_mul_f32_e32 v5, v23, v19
	v_mul_f32_e32 v8, v9, v5
	v_mov_b32_e32 v5, v3
	v_cvt_pk_fp8_f32 v5, v7, v8
	v_mul_f32_e32 v7, v20, v19
	v_mul_f32_e32 v8, v21, v19
	v_mul_f32_e32 v7, v10, v7
	v_mul_f32_e32 v8, v11, v8
	v_cvt_pk_fp8_f32 v5, v7, v8 op_sel:[0,0,1]
	v_mul_f32_e32 v7, v18, v19
	v_permlane32_swap_b32_e32 v4, v5
	s_waitcnt vmcnt(1)
	s_nop 1
	v_mov_b32_e32 v8, v226
	v_mov_b32_e32 v9, v227
	v_mov_b32_e32 v10, v228
	v_mov_b32_e32 v11, v229
	v_mul_f32_e32 v2, v8, v2
	v_mul_f32_e32 v8, v9, v7
	v_mov_b32_e32 v7, v3
	v_cvt_pk_fp8_f32 v7, v2, v8
	v_mul_f32_e32 v2, v12, v19
	v_mul_f32_e32 v8, v13, v19
	v_mul_f32_e32 v2, v10, v2
	v_mul_f32_e32 v8, v11, v8
	v_cvt_pk_fp8_f32 v7, v2, v8 op_sel:[0,0,1]
	s_nop 1
	v_permlane32_swap_b32_e32 v6, v7
	global_store_dwordx4 v[14:15], v[4:7], off offset:96
	s_cbranch_vccz .LBB0_359

.Lconv_body:
	v_lshlrev_b32_e32 v97, 16, v92
	v_cndmask_b32_e64 v197, 1.0, 0, vcc
	v_mul_f32_e32 v96, v4, v161
	v_lshlrev_b32_e32 v107, 16, v88
	v_and_b32_e32 v123, 0xffff0000, v88
	v_lshlrev_b32_e32 v103, 16, v90
	v_and_b32_e32 v119, 0xffff0000, v90
	v_lshlrev_b32_e32 v2, 16, v84
	v_and_b32_e32 v80, 0xffff0000, v84
	v_lshlrev_b32_e32 v88, 16, v85
	v_and_b32_e32 v90, 0xffff0000, v85
	v_pk_mul_f32 v[114:115], v[114:115], v[96:97]
	v_pk_mul_f32 v[84:85], v[138:139], v[196:197]
	v_lshlrev_b32_e32 v111, 16, v98
	v_add_f32_e32 v84, v84, v114
	v_and_b32_e32 v129, 0xffff0000, v98
	v_lshlrev_b32_e32 v109, 16, v99
	v_and_b32_e32 v125, 0xffff0000, v99
	v_and_b32_e32 v99, 0xffff0000, v92
	v_fmac_f32_e32 v84, v85, v115
	v_mul_f32_e32 v98, v5, v161
	v_mov_b32_e32 v193, v197
	v_mul_f32_e32 v2, v84, v2
	v_pk_mul_f32 v[150:151], v[144:145], v[98:99]
	v_pk_mul_f32 v[84:85], v[12:13], v[192:193]
	v_lshlrev_b32_e32 v157, 16, v93
	v_add_f32_e32 v84, v84, v150
	v_fmac_f32_e32 v84, v85, v151
	v_mul_f32_e32 v156, v6, v161
	v_mov_b32_e32 v191, v197
	v_mul_f32_e32 v80, v84, v80
	v_pk_mul_f32 v[112:113], v[112:113], v[156:157]
	v_pk_mul_f32 v[84:85], v[136:137], v[190:191]
	v_and_b32_e32 v93, 0xffff0000, v93
	v_add_f32_e32 v84, v84, v112
	v_fmac_f32_e32 v84, v85, v113
	v_mul_f32_e32 v92, v7, v161
	v_mov_b32_e32 v189, v197
	v_mul_f32_e32 v88, v84, v88
	v_pk_mul_f32 v[156:157], v[132:133], v[92:93]
	v_pk_mul_f32 v[84:85], v[14:15], v[188:189]
	v_lshlrev_b32_e32 v159, 16, v94
	v_add_f32_e32 v84, v84, v156
	v_fmac_f32_e32 v84, v85, v157
	v_mul_f32_e32 v158, v8, v161
	v_mov_b32_e32 v187, v197
	v_mul_f32_e32 v90, v84, v90
	v_pk_mul_f32 v[110:111], v[110:111], v[158:159]
	v_pk_mul_f32 v[84:85], v[134:135], v[186:187]
	v_and_b32_e32 v195, 0xffff0000, v94
	v_add_f32_e32 v84, v84, v110
	v_lshlrev_b32_e32 v94, 16, v86
	v_fmac_f32_e32 v84, v85, v111
	v_mul_f32_e32 v194, v9, v161
	v_mov_b32_e32 v185, v197
	v_mul_f32_e32 v92, v84, v94
	v_pk_mul_f32 v[158:159], v[128:129], v[194:195]
	v_pk_mul_f32 v[84:85], v[16:17], v[184:185]
	v_lshlrev_b32_e32 v199, 16, v95
	v_add_f32_e32 v84, v84, v158
	v_and_b32_e32 v86, 0xffff0000, v86
	v_fmac_f32_e32 v84, v85, v159
	v_mul_f32_e32 v198, v10, v161
	v_mov_b32_e32 v183, v197
	v_mul_f32_e32 v96, v80, v80
	v_mul_f32_e32 v86, v84, v86
	v_pk_mul_f32 v[108:109], v[108:109], v[198:199]
	v_pk_mul_f32 v[84:85], v[130:131], v[182:183]
	v_fmac_f32_e32 v96, v2, v2
	v_add_f32_e32 v84, v84, v108
	v_and_b32_e32 v95, 0xffff0000, v95
	v_lshlrev_b32_e32 v163, 16, v87
	v_fmac_f32_e32 v96, v88, v88
	v_fmac_f32_e32 v84, v85, v109
	v_mul_f32_e32 v94, v11, v161
	v_mov_b32_e32 v177, v197
	v_fmac_f32_e32 v96, v90, v90
	v_mul_f32_e32 v98, v84, v163
	v_pk_mul_f32 v[194:195], v[124:125], v[94:95]
	v_pk_mul_f32 v[84:85], v[18:19], v[176:177]
	v_fmac_f32_e32 v96, v92, v92
	v_add_f32_e32 v84, v84, v194
	v_and_b32_e32 v87, 0xffff0000, v87
	v_fmac_f32_e32 v96, v86, v86
	v_fmac_f32_e32 v84, v85, v195
	v_fmac_f32_e32 v96, v98, v98
	v_mul_f32_e32 v99, v84, v87
	v_fmac_f32_e32 v96, v99, v99
	v_lshlrev_b32_e32 v87, 16, v82
	v_mov_b32_e32 v175, v197
	v_add_f32_dpp v84, v96, v96 quad_perm:[1,0,3,2] row_mask:0xf bank_mask:0xf bound_ctrl:1
	v_mov_b32_e32 v173, v197
	v_mov_b32_e32 v171, v197
	v_add_f32_dpp v84, v84, v84 quad_perm:[2,3,0,1] row_mask:0xf bank_mask:0xf bound_ctrl:1
	v_mov_b32_e32 v169, v197
	v_mov_b32_e32 v167, v197
	v_add_f32_dpp v84, v84, v84 row_ror:4 row_mask:0xf bank_mask:0xf bound_ctrl:1
	v_mov_b32_e32 v165, v197
	v_mov_b32_e32 v163, v197
	v_add_f32_dpp v84, v84, v84 row_ror:8 row_mask:0xf bank_mask:0xf bound_ctrl:1
	v_fmamk_f32 v84, v84, 0x3c000000, v207
	v_mul_f32_e32 v85, 0x4f800000, v84
	v_cmp_gt_f32_e32 vcc, s10, v84
	v_lshlrev_b32_e32 v110, 16, v55
	v_and_b32_e32 v55, 0xffff0000, v55
	v_cndmask_b32_e32 v84, v84, v85, vcc
	v_sqrt_f32_e32 v93, v84
	v_lshlrev_b32_e32 v85, 16, v81
	v_and_b32_e32 v81, 0xffff0000, v81
	s_mov_b32 s4, 0x20b00000
	v_add_u32_e32 v94, -1, v93
	v_fma_f32 v95, -v94, v93, v84
	v_cmp_ge_f32_e64 s[40:41], 0, v95
	v_add_u32_e32 v95, 1, v93
	v_mov_b32_e32 v114, v196
	v_cndmask_b32_e64 v94, v93, v94, s[40:41]
	v_fma_f32 v93, -v95, v93, v84
	v_cmp_lt_f32_e64 s[40:41], 0, v93
	v_mov_b32_e32 v144, v192
	v_mov_b32_e32 v112, v190
	v_cndmask_b32_e64 v93, v94, v95, s[40:41]
	v_mul_f32_e32 v94, 0x37800000, v93
	v_cndmask_b32_e32 v93, v93, v94, vcc
	v_cmp_class_f32_e32 vcc, v84, v208
	v_lshlrev_b32_e32 v95, 16, v83
	v_and_b32_e32 v83, 0xffff0000, v83
	v_cndmask_b32_e32 v84, v93, v84, vcc
	v_div_scale_f32 v94, s[8:9], v84, v84, 1.0
	v_rcp_f32_e32 v96, v94
	v_and_b32_e32 v93, 0xffff0000, v82
	v_mov_b32_e32 v132, v188
	v_mov_b32_e32 v128, v184
	v_fma_f32 v82, -v94, v96, 1.0
	v_fmac_f32_e32 v96, v82, v96
	v_div_scale_f32 v82, vcc, 1.0, v84, 1.0
	v_mul_f32_e32 v97, v82, v96
	v_fma_f32 v108, -v94, v97, v82
	v_fmac_f32_e32 v97, v108, v96
	v_fma_f32 v82, -v94, v97, v82
	v_div_fmas_f32 v82, v82, v96, v97
	v_div_fixup_f32 v108, v82, v84, 1.0
	v_mul_f32_e32 v2, v2, v108
	v_mul_f32_e32 v80, v80, v108
	v_mul_f32_e32 v2, v20, v2
	v_mul_f32_e32 v80, v21, v80
	v_mov_b32_e32 v96, v3
	v_cvt_pk_fp8_f32 v96, v2, v80
	v_mul_f32_e32 v2, v88, v108
	v_mul_f32_e32 v80, v90, v108
	v_mul_f32_e32 v2, v22, v2
	v_mul_f32_e32 v80, v23, v80
	v_cvt_pk_fp8_f32 v96, v2, v80 op_sel:[0,0,1]
	v_mul_f32_e32 v2, v92, v108
	v_mul_f32_e32 v80, v86, v108
	v_mul_f32_e32 v2, v24, v2
	v_mul_f32_e32 v80, v25, v80
	v_mov_b32_e32 v97, v3
	v_mul_f32_e32 v90, v28, v161
	v_cvt_pk_fp8_f32 v97, v2, v80
	v_lshlrev_b32_e32 v2, 16, v52
	v_and_b32_e32 v80, 0xffff0000, v52
	v_lshlrev_b32_e32 v82, 16, v53
	v_and_b32_e32 v86, 0xffff0000, v53
	v_pk_mul_f32 v[106:107], v[106:107], v[90:91]
	v_pk_mul_f32 v[52:53], v[148:149], v[174:175]
	v_mul_f32_e32 v88, v29, v161
	v_add_f32_e32 v52, v52, v106
	v_fmac_f32_e32 v52, v53, v107
	v_mul_f32_e32 v2, v52, v2
	v_pk_mul_f32 v[198:199], v[122:123], v[88:89]
	v_pk_mul_f32 v[52:53], v[36:37], v[172:173]
	v_mul_f32_e32 v84, v30, v161
	v_add_f32_e32 v52, v52, v198
	v_fmac_f32_e32 v52, v53, v199
	v_mul_f32_e32 v88, v52, v80
	v_pk_mul_f32 v[104:105], v[104:105], v[84:85]
	v_pk_mul_f32 v[52:53], v[146:147], v[170:171]
	v_mul_f32_e32 v80, v31, v161
	v_add_f32_e32 v52, v52, v104
	v_fmac_f32_e32 v52, v53, v105
	v_mul_f32_e32 v84, v52, v82
	v_pk_mul_f32 v[200:201], v[120:121], v[80:81]
	v_pk_mul_f32 v[52:53], v[38:39], v[168:169]
	v_lshlrev_b32_e32 v92, 16, v54
	v_add_f32_e32 v52, v52, v200
	v_fmac_f32_e32 v52, v53, v201
	v_mul_f32_e32 v80, v52, v86
	v_mul_f32_e32 v86, v32, v161
	v_pk_mul_f32 v[102:103], v[102:103], v[86:87]
	v_pk_mul_f32 v[52:53], v[142:143], v[166:167]
	v_and_b32_e32 v54, 0xffff0000, v54
	v_add_f32_e32 v52, v52, v102
	v_fmac_f32_e32 v52, v53, v103
	v_mul_f32_e32 v81, v52, v92
	v_mul_f32_e32 v92, v33, v161
	v_pk_mul_f32 v[202:203], v[118:119], v[92:93]
	v_pk_mul_f32 v[52:53], v[40:41], v[164:165]
	v_mul_f32_e32 v94, v34, v161
	v_add_f32_e32 v52, v52, v202
	v_fmac_f32_e32 v52, v53, v203
	v_mul_f32_e32 v89, v88, v88
	v_mul_f32_e32 v85, v52, v54
	v_pk_mul_f32 v[100:101], v[100:101], v[94:95]
	v_pk_mul_f32 v[52:53], v[140:141], v[162:163]
	v_fmac_f32_e32 v89, v2, v2
	v_add_f32_e32 v52, v52, v100
	v_fmac_f32_e32 v89, v84, v84
	v_fmac_f32_e32 v52, v53, v101
	v_mul_f32_e32 v82, v35, v161
	v_mov_b32_e32 v161, v197
	v_fmac_f32_e32 v89, v80, v80
	v_mul_f32_e32 v86, v52, v110
	v_pk_mul_f32 v[204:205], v[116:117], v[82:83]
	v_pk_mul_f32 v[52:53], v[42:43], v[160:161]
	v_fmac_f32_e32 v89, v81, v81
	v_add_f32_e32 v52, v52, v204
	v_fmac_f32_e32 v89, v85, v85
	v_fmac_f32_e32 v52, v53, v205
	v_fmac_f32_e32 v89, v86, v86
	v_mul_f32_e32 v82, v52, v55
	v_fmac_f32_e32 v89, v82, v82
	v_mul_f32_e32 v54, v98, v108
	v_mul_f32_e32 v55, v99, v108
	v_add_f32_dpp v52, v89, v89 quad_perm:[1,0,3,2] row_mask:0xf bank_mask:0xf bound_ctrl:1
	v_mul_f32_e32 v54, v26, v54
	s_waitcnt vmcnt(3)
	v_mov_b64_e32 v[94:95], v[66:67]
	v_add_f32_dpp v52, v52, v52 quad_perm:[2,3,0,1] row_mask:0xf bank_mask:0xf bound_ctrl:1
	v_mov_b64_e32 v[92:93], v[64:65]
	v_mov_b32_e32 v110, v186
	v_add_f32_dpp v52, v52, v52 row_ror:4 row_mask:0xf bank_mask:0xf bound_ctrl:1
	v_mov_b32_e32 v108, v182
	v_mov_b32_e32 v124, v176
	v_add_f32_dpp v52, v52, v52 row_ror:8 row_mask:0xf bank_mask:0xf bound_ctrl:1
	v_fmamk_f32 v52, v52, 0x3c000000, v207
	v_mul_f32_e32 v53, 0x4f800000, v52
	v_cmp_gt_f32_e32 vcc, s10, v52
	v_mov_b32_e32 v106, v174
	v_mov_b32_e32 v122, v172
	v_cndmask_b32_e32 v52, v52, v53, vcc
	v_sqrt_f32_e32 v53, v52
	v_mov_b32_e32 v104, v170
	v_mov_b32_e32 v120, v168
	v_mov_b32_e32 v102, v166
	v_add_u32_e32 v83, -1, v53
	v_fma_f32 v87, -v83, v53, v52
	v_cmp_ge_f32_e64 s[40:41], 0, v87
	v_add_u32_e32 v87, 1, v53
	v_mov_b32_e32 v118, v164
	v_cndmask_b32_e64 v83, v53, v83, s[40:41]
	v_fma_f32 v53, -v87, v53, v52
	v_cmp_lt_f32_e64 s[40:41], 0, v53
	v_mov_b32_e32 v100, v162
	v_mov_b32_e32 v116, v160
	v_cndmask_b32_e64 v53, v83, v87, s[40:41]
	v_mul_f32_e32 v83, 0x37800000, v53
	v_cndmask_b32_e32 v53, v53, v83, vcc
	v_cmp_class_f32_e32 vcc, v52, v208
	s_nop 1
	v_cndmask_b32_e32 v83, v53, v52, vcc
	v_div_scale_f32 v87, s[8:9], v83, v83, 1.0
	v_rcp_f32_e32 v89, v87
	v_mul_f32_e32 v52, v27, v55
	v_cvt_pk_fp8_f32 v97, v54, v52 op_sel:[0,0,1]
	v_lshl_add_u64 v[52:53], s[0:1], 0, v[152:153]
	v_fma_f32 v54, -v87, v89, 1.0
	v_fmac_f32_e32 v89, v54, v89
	v_div_scale_f32 v54, vcc, 1.0, v83, 1.0
	v_mul_f32_e32 v55, v54, v89
	v_fma_f32 v90, -v87, v55, v54
	v_fmac_f32_e32 v55, v90, v89
	v_fma_f32 v54, -v87, v55, v54
	v_div_fmas_f32 v54, v54, v89, v55
	v_div_fixup_f32 v83, v54, v83, 1.0
	v_mul_f32_e32 v2, v2, v83
	v_mul_f32_e32 v54, v88, v83
	s_waitcnt lgkmcnt(1)
	v_mul_f32_e32 v2, v44, v2
	v_mul_f32_e32 v55, v45, v54
	v_mov_b32_e32 v54, v3
	v_cvt_pk_fp8_f32 v54, v2, v55
	v_mul_f32_e32 v2, v84, v83
	v_mul_f32_e32 v55, v80, v83
	v_mul_f32_e32 v2, v46, v2
	v_mul_f32_e32 v55, v47, v55
	v_cvt_pk_fp8_f32 v54, v2, v55 op_sel:[0,0,1]
	v_mul_f32_e32 v2, v81, v83
	v_mul_f32_e32 v55, v85, v83
	s_waitcnt lgkmcnt(0)
	v_mul_f32_e32 v2, v48, v2
	v_mul_f32_e32 v80, v49, v55
	v_mov_b32_e32 v55, v3
	v_cvt_pk_fp8_f32 v55, v2, v80
	v_mul_f32_e32 v2, v86, v83
	v_mul_f32_e32 v80, v82, v83
	v_mul_f32_e32 v2, v50, v2
	v_mul_f32_e32 v80, v51, v80
	v_cvt_pk_fp8_f32 v55, v2, v80 op_sel:[0,0,1]
	v_add_co_u32_e32 v52, vcc, s4, v52
	s_mov_b64 s[8:9], 0x800
	s_nop 0
	v_addc_co_u32_e32 v53, vcc, 0, v53, vcc
	global_store_dwordx2 v[52:53], v[96:97], off offset:1024
	global_store_dwordx2 v[52:53], v[54:55], off offset:1536
	v_lshl_add_u64 v[152:153], v[152:153], 0, s[8:9]
	s_mov_b64 s[8:9], 0x2400
	s_waitcnt vmcnt(2)
	v_mov_b64_e32 v[52:53], v[76:77]
	v_mov_b64_e32 v[86:87], v[74:75]
	v_mov_b64_e32 v[98:99], v[58:59]
	v_mov_b64_e32 v[90:91], v[62:63]
	v_mov_b64_e32 v[82:83], v[70:71]
	v_lshl_add_u64 v[154:155], v[154:155], 0, s[8:9]
	s_andn2_b64 vcc, exec, s[42:43]
	v_mov_b64_e32 v[54:55], v[78:79]
	v_mov_b64_e32 v[84:85], v[72:73]
	s_mov_b32 s4, s5
	v_mov_b64_e32 v[96:97], v[56:57]
	v_mov_b64_e32 v[88:89], v[60:61]
	v_mov_b64_e32 v[80:81], v[68:69]
	s_cbranch_vccz .LBB0_369
.LBB0_367:
	s_add_i32 s5, s4, 1
	s_cmp_ge_i32 s5, s6
	s_cselect_b64 s[42:43], -1, 0
	v_mov_b32_e32 v160, v205
	v_mov_b32_e32 v162, v101
	v_mov_b32_e32 v164, v203
	v_mov_b32_e32 v166, v103
	v_mov_b32_e32 v168, v201
	v_mov_b32_e32 v170, v105
	v_mov_b32_e32 v172, v199
	v_mov_b32_e32 v174, v107
	v_mov_b32_e32 v176, v195
	v_mov_b32_e32 v182, v109
	v_mov_b32_e32 v184, v159
	v_mov_b32_e32 v186, v111
	v_mov_b32_e32 v188, v157
	v_mov_b32_e32 v190, v113
	v_mov_b32_e32 v192, v151
	v_mov_b32_e32 v196, v115
	s_and_b64 vcc, exec, s[42:43]
	s_cbranch_vccnz .LBB0_366
	s_min_i32 s8, s4, 0x41fd
	s_add_i32 s8, s8, 2
	v_mad_i64_i32 v[60:61], s[8:9], s8, v215, v[126:127]
	v_add_co_u32_e32 v68, vcc, 0x1000, v60
	v_lshl_add_u64 v[72:73], s[0:1], 0, v[154:155]
	s_nop 0
	v_addc_co_u32_e32 v69, vcc, 0, v61, vcc
	global_load_dwordx4 v[56:59], v[60:61], off offset:2048
	s_nop 0
	global_load_dwordx4 v[60:63], v[60:61], off offset:3072
	s_nop 0
	global_load_dwordx4 v[64:67], v[68:69], off
	s_nop 0
	global_load_dwordx4 v[68:71], v[68:69], off offset:1024
	v_add_co_u32_e32 v76, vcc, 0x17600000, v72
	s_nop 1
	v_addc_co_u32_e32 v77, vcc, 0, v73, vcc
	global_load_dwordx4 v[72:75], v[76:77], off
	s_nop 0
	global_load_dwordx4 v[76:79], v[76:77], off offset:1024
	s_waitcnt vmcnt(6)
	s_and_b32 s8, s4, 0x1fff
	s_cmpk_eq_i32 s8, 0x1fff
	s_cselect_b64 s[8:9], -1, 0
	s_and_b32 s27, s4, 0xff
	s_cmpk_eq_i32 s27, 0xff
	s_cselect_b64 s[40:41], -1, 0
	s_cmpk_lt_i32 s4, 0x4000
	s_movk_i32 s27, 0x1fff
	s_cselect_b32 s27, s27, 0xff
	v_lshlrev_b32_e32 v105, 16, v89
	v_and_b32_e32 v121, 0xffff0000, v89
	v_lshlrev_b32_e32 v101, 16, v91
	v_and_b32_e32 v117, 0xffff0000, v91
	v_lshlrev_b32_e32 v91, 16, v80
	v_and_b32_e32 v89, 0xffff0000, v80
	v_cndmask_b32_e64 v2, 0, 1, s[40:41]
	v_cndmask_b32_e64 v80, 0, 1, s[8:9]
	s_cselect_b64 vcc, -1, 0
	s_and_b32 s4, s27, s4
	v_cndmask_b32_e32 v2, v2, v80, vcc
	s_cmp_eq_u32 s4, 0
	s_cselect_b64 s[8:9], -1, 0
	v_and_b32_e32 v2, 1, v2
	v_cndmask_b32_e64 v161, 1.0, 0, s[8:9]
	v_cmp_eq_u32_e32 vcc, 1, v2
	v_lshlrev_b32_e32 v115, 16, v96
	v_and_b32_e32 v145, 0xffff0000, v96
	v_lshlrev_b32_e32 v113, 16, v97
	v_and_b32_e32 v133, 0xffff0000, v97
	s_branch .Lconv_body
